# speedup vs baseline: 1.0034x; 1.0034x over previous
_Z6conv_kILi64ELi128ELi20ELi128ELi4ELi4ELb1EEvPKDF16_S1_PKfS3_PDF16_S4_S1_fS3_S3_S3_S3_:
	s_load_dwordx2 s[22:23], s[0:1], 0x8
	s_load_dwordx8 s[24:31], s[0:1], 0x40
	v_readfirstlane_b32 s34, v0
	s_lshr_b32 s35, s34, 6
	v_lshlrev_b32_e32 v1, 3, v0
	v_and_b32_e32 v2, 48, v0
	s_and_b32 s33, s2, 3
	v_bitop3_b32 v2, v1, v2, 56 bitop3:0x6c
	s_lshl_b32 s5, s35, 10
	v_and_b32_e32 v1, 0x1c0, v1
	s_and_b32 s4, s2, 56
	v_or3_b32 v18, s5, v1, v2
	v_and_b32_e32 v1, 7, v0
	s_mul_i32 s5, s33, 5
	v_or_b32_e32 v97, 0x200, v0
	s_lshl_b32 s3, s2, 3
	v_lshlrev_b32_e32 v19, 5, v1
	s_add_i32 s4, s4, s5
	v_mul_u32_u24_e32 v23, 0x283, v97
	s_and_b32 s3, s3, 32
	s_waitcnt lgkmcnt(0)
	global_load_dwordx4 v[2:5], v19, s[26:27] offset:16
	global_load_dwordx4 v[6:9], v19, s[28:29] offset:16
	global_load_dwordx4 v[10:13], v19, s[26:27]
	global_load_dwordx4 v[14:17], v19, s[28:29]
	s_add_i32 s20, s4, -9
	v_mul_u32_u24_e32 v19, 0xa1, v0
	s_movk_i32 s4, 0xffcd
	v_lshrrev_b32_e32 v23, 18, v23
	s_add_i32 s21, s3, -9
	v_lshrrev_b32_e32 v37, 3, v0
	v_mul_i32_i24_sdwa v20, v19, s4 dst_sel:DWORD dst_unused:UNUSED_PAD src0_sel:WORD_1 src1_sel:DWORD
	v_lshrrev_b32_e32 v50, 3, v97
	v_mul_i32_i24_e32 v24, 0xffffffcd, v23
	v_add_u32_sdwa v19, s20, v19 dst_sel:DWORD dst_unused:UNUSED_PAD src0_sel:DWORD src1_sel:WORD_1
	v_add3_u32 v20, s21, v37, v20
	v_add_u32_e32 v23, s20, v23
	v_add3_u32 v24, s21, v50, v24
	v_max_u32_e32 v21, v19, v20
	v_max_u32_e32 v25, v23, v24
	v_cmp_gt_u32_e64 s[16:17], 64, v21
	v_cmp_lt_u32_e64 s[14:15], 63, v25
	s_and_b32 s28, s2, 0xffffffc0
	v_cndmask_b32_e64 v19, 0, v19, s[16:17]
	v_cndmask_b32_e64 v23, v23, 0, s[14:15]
	v_or_b32_e32 v19, s28, v19
	v_cndmask_b32_e64 v20, 0, v20, s[16:17]
	v_or_b32_e32 v23, s28, v23
	v_cndmask_b32_e64 v24, v24, 0, s[14:15]
	v_lshl_add_u32 v20, v19, 6, v20
	v_cndmask_b32_e64 v19, 0, 1, s[16:17]
	v_lshl_add_u32 v24, v23, 6, v24
	v_cndmask_b32_e64 v23, 2, 0, s[14:15]
	v_or_b32_e32 v102, 0x400, v0
	v_or_b32_e32 v19, v23, v19
	v_mul_u32_u24_e32 v23, 0xa0b, v102
	v_lshrrev_b32_e32 v23, 20, v23
	v_lshrrev_b32_e32 v51, 3, v102
	v_mul_i32_i24_e32 v26, 0xffffffcd, v23
	v_add_u32_e32 v23, s20, v23
	v_add3_u32 v26, s21, v51, v26
	v_max_u32_e32 v27, v23, v26
	v_cmp_lt_u32_e64 s[12:13], 63, v27
	v_or_b32_e32 v103, 0x600, v0
	v_lshrrev_b32_e32 v52, 3, v103
	v_cndmask_b32_e64 v23, v23, 0, s[12:13]
	v_or_b32_e32 v23, s28, v23
	v_cndmask_b32_e64 v26, v26, 0, s[12:13]
	v_lshl_add_u32 v26, v23, 6, v26
	v_ashrrev_i32_e32 v27, 31, v26
	v_lshl_add_u64 v[38:39], v[26:27], 2, s[24:25]
	v_mul_u32_u24_e32 v26, 0xa0b, v103
	v_lshrrev_b32_e32 v26, 20, v26
	v_mul_i32_i24_e32 v27, 0xffffffcd, v26
	v_add_u32_e32 v26, s20, v26
	v_add3_u32 v27, s21, v52, v27
	v_max_u32_e32 v28, v26, v27
	v_cmp_lt_u32_e64 s[10:11], 63, v28
	v_cndmask_b32_e64 v23, 4, 0, s[12:13]
	v_or_b32_e32 v104, 0x800, v0
	v_cndmask_b32_e64 v26, v26, 0, s[10:11]
	v_or_b32_e32 v26, s28, v26
	v_cndmask_b32_e64 v27, v27, 0, s[10:11]
	v_lshl_add_u32 v26, v26, 6, v27
	v_ashrrev_i32_e32 v27, 31, v26
	v_lshl_add_u64 v[40:41], v[26:27], 2, s[24:25]
	v_cndmask_b32_e64 v26, 8, 0, s[10:11]
	v_or3_b32 v19, v19, v23, v26
	v_mul_u32_u24_e32 v23, 0x1415, v104
	v_lshrrev_b32_e32 v23, 21, v23
	v_lshrrev_b32_e32 v35, 3, v104
	v_mul_i32_i24_e32 v26, 0xffffffcd, v23
	v_add_u32_e32 v23, s20, v23
	v_add3_u32 v26, s21, v35, v26
	v_max_u32_e32 v27, v23, v26
	v_cmp_lt_u32_e64 s[8:9], 63, v27
	v_or_b32_e32 v105, 0xa00, v0
	v_lshrrev_b32_e32 v33, 3, v105
	v_cndmask_b32_e64 v23, v23, 0, s[8:9]
	v_or_b32_e32 v23, s28, v23
	v_cndmask_b32_e64 v26, v26, 0, s[8:9]
	v_lshl_add_u32 v26, v23, 6, v26
	v_ashrrev_i32_e32 v27, 31, v26
	v_lshl_add_u64 v[42:43], v[26:27], 2, s[24:25]
	v_mul_u32_u24_e32 v26, 0x1415, v105
	v_lshrrev_b32_e32 v26, 21, v26
	v_mul_i32_i24_e32 v27, 0xffffffcd, v26
	v_add_u32_e32 v26, s20, v26
	v_add3_u32 v27, s21, v33, v27
	v_max_u32_e32 v28, v26, v27
	v_cmp_lt_u32_e64 s[6:7], 63, v28
	v_cndmask_b32_e64 v23, 16, 0, s[8:9]
	v_or_b32_e32 v106, 0xc00, v0
	v_cndmask_b32_e64 v26, v26, 0, s[6:7]
	v_or_b32_e32 v26, s28, v26
	v_cndmask_b32_e64 v27, v27, 0, s[6:7]
	v_lshl_add_u32 v26, v26, 6, v27
	v_ashrrev_i32_e32 v27, 31, v26
	v_lshl_add_u64 v[44:45], v[26:27], 2, s[24:25]
	v_cndmask_b32_e64 v26, 32, 0, s[6:7]
	v_or3_b32 v30, v19, v23, v26
	v_mul_u32_u24_e32 v19, 0x1415, v106
	v_lshrrev_b32_e32 v19, 21, v19
	v_lshrrev_b32_e32 v31, 3, v106
	v_mul_i32_i24_e32 v23, 0xffffffcd, v19
	v_add_u32_e32 v19, s20, v19
	v_add3_u32 v23, s21, v31, v23
	v_max_u32_e32 v26, v19, v23
	v_cmp_gt_u32_e32 vcc, 64, v26
	v_or_b32_e32 v107, 0xe00, v0
	v_ashrrev_i32_e32 v21, 31, v20
	v_cndmask_b32_e32 v19, 0, v19, vcc
	v_or_b32_e32 v19, s28, v19
	v_cndmask_b32_e32 v23, 0, v23, vcc
	v_lshl_add_u32 v26, v19, 6, v23
	v_mul_u32_u24_e32 v23, 0x1415, v107
	v_ashrrev_i32_e32 v27, 31, v26
	v_lshrrev_b32_e32 v23, 21, v23
	v_lshl_add_u64 v[46:47], v[26:27], 2, s[24:25]
	v_lshrrev_b32_e32 v26, 3, v107
	v_mul_i32_i24_e32 v27, 0xffffffcd, v23
	v_add_u32_e32 v23, s20, v23
	v_add3_u32 v27, s21, v26, v27
	v_max_u32_e32 v28, v23, v27
	v_cndmask_b32_e64 v19, 0, 64, vcc
	v_cmp_gt_u32_e32 vcc, 64, v28
	v_lshl_add_u64 v[20:21], v[20:21], 2, s[24:25]
	v_ashrrev_i32_e32 v25, 31, v24
	v_cndmask_b32_e32 v23, 0, v23, vcc
	v_or_b32_e32 v23, s28, v23
	v_cndmask_b32_e32 v27, 0, v27, vcc
	v_lshl_add_u32 v28, v23, 6, v27
	v_ashrrev_i32_e32 v29, 31, v28
	s_load_dword s26, s[30:31], 0x0
	v_lshl_add_u64 v[24:25], v[24:25], 2, s[24:25]
	v_lshl_add_u64 v[48:49], v[28:29], 2, s[24:25]
	global_load_dword v53, v[20:21], off
	global_load_dword v54, v[24:25], off
	global_load_dword v55, v[38:39], off
	global_load_dword v56, v[40:41], off
	global_load_dword v57, v[42:43], off
	global_load_dword v36, v[44:45], off
	global_load_dword v34, v[46:47], off
	global_load_dword v29, v[48:49], off
	v_mov_b32_e32 v20, 0x80
	v_cndmask_b32_e32 v20, 0, v20, vcc
	v_or_b32_e32 v32, v19, v20
	v_or_b32_e32 v20, 0x1000, v0
	v_mul_u32_u24_e32 v21, 0x2829, v20
	v_lshrrev_b32_e32 v21, 22, v21
	v_lshrrev_b32_e32 v24, 3, v20
	v_mul_i32_i24_e32 v23, 0xffffffcd, v21
	v_add_u32_e32 v28, s20, v21
	s_movk_i32 s4, 0x1320
	v_add3_u32 v27, s21, v24, v23
	v_cmp_gt_u32_e64 s[4:5], s4, v20
	v_cmp_gt_u32_e32 vcc, 64, v28
	s_and_b64 s[18:19], s[4:5], vcc
	v_cmp_gt_u32_e32 vcc, 64, v27
	v_mov_b32_e32 v20, 0x100
	s_and_b64 s[18:19], s[18:19], vcc
	v_cndmask_b32_e64 v23, 0, v20, s[18:19]
	v_or_b32_e32 v20, 0x1200, v0
	v_lshrrev_b32_e32 v21, 3, v20
	v_mul_u32_u24_e32 v20, 0x2829, v20
	v_lshrrev_b32_e32 v20, 22, v20
	v_mul_i32_i24_e32 v25, 0xffffffcd, v20
	v_add_u32_e32 v20, s20, v20
	s_movk_i32 s20, 0x120
	v_add3_u32 v25, s21, v21, v25
	v_cmp_gt_u32_e32 vcc, s20, v0
	v_cmp_gt_u32_e64 s[20:21], 64, v20
	s_and_b64 s[30:31], vcc, s[20:21]
	v_cmp_gt_u32_e64 s[20:21], 64, v25
	s_and_b64 s[20:21], s[30:31], s[20:21]
	s_lshl_b32 s36, s35, 11
	v_cndmask_b32_e64 v20, 0, v20, s[20:21]
	v_or_b32_e32 v20, s28, v20
	v_cndmask_b32_e64 v25, 0, v25, s[20:21]
	v_lshl_add_u32 v38, v20, 6, v25
	v_mov_b32_e32 v25, 0x200
	v_or_b32_e32 v19, v32, v30
	v_ashrrev_i32_e32 v39, 31, v38
	v_cndmask_b32_e64 v25, 0, v25, s[20:21]
	s_add_i32 s27, s36, 0x14000
	s_mul_i32 s20, s33, 0x190000
	v_lshl_add_u64 v[38:39], v[38:39], 2, s[24:25]
	v_or3_b32 v25, v23, v25, v19
	v_mov_b32_e32 v19, 0
	s_add_u32 s20, s22, s20
	global_load_dword v20, v[38:39], off
	s_addc_u32 s21, s23, 0
	v_lshlrev_b64 v[38:39], 1, v[18:19]
	v_lshl_add_u64 v[40:41], s[20:21], 0, v[38:39]
	s_mov_b32 m0, s27
	s_mov_b64 s[30:31], 0x400
	global_load_lds_dwordx4 v[40:41], off
	s_add_i32 m0, s36, 0x14400
	v_lshl_add_u64 v[40:41], v[40:41], 0, s[30:31]
	s_add_u32 s30, s20, 0x50000
	s_addc_u32 s31, s21, 0
	global_load_lds_dwordx4 v[40:41], off
	s_add_i32 m0, s36, 0x18000
	v_lshl_add_u64 v[40:41], s[30:31], 0, v[38:39]
	v_or_b32_e32 v22, 0x200, v18
	v_mov_b32_e32 v23, v19
	global_load_lds_dwordx4 v[40:41], off
	s_add_i32 m0, s36, 0x18400
	v_lshlrev_b64 v[22:23], 1, v[22:23]
	s_add_u32 s20, s20, 0xa0000
	v_lshl_add_u64 v[40:41], s[30:31], 0, v[22:23]
	s_addc_u32 s21, s21, 0
	global_load_lds_dwordx4 v[40:41], off
	s_add_i32 m0, s36, 0x1c000
	v_lshl_add_u64 v[38:39], s[20:21], 0, v[38:39]
	global_load_lds_dwordx4 v[38:39], off
	v_lshl_add_u64 v[22:23], s[20:21], 0, v[22:23]
	s_add_i32 m0, s36, 0x1c400
	s_movk_i32 s29, 0x80
	global_load_lds_dwordx4 v[22:23], off
	s_waitcnt vmcnt(6)
	v_fma_f32 v22, v53, v10, v14
	s_waitcnt lgkmcnt(0)
	v_mul_f32_e32 v23, s26, v22
	v_cmp_le_f32_e64 s[20:21], 0, v22
	s_nop 1
	v_cndmask_b32_e64 v22, v23, v22, s[20:21]
	v_fma_f32 v23, v53, v11, v15
	v_mul_f32_e32 v38, s26, v23
	v_cmp_le_f32_e64 s[20:21], 0, v23
	v_cvt_f16_f32_e32 v22, v22
	v_cndmask_b32_e64 v22, 0, v22, s[16:17]
	v_cndmask_b32_e64 v23, v38, v23, s[20:21]
	v_fma_f32 v38, v53, v12, v16
	v_mul_f32_e32 v39, s26, v38
	v_cmp_le_f32_e64 s[20:21], 0, v38
	v_cvt_f16_f32_e32 v23, v23
	v_cndmask_b32_e64 v23, 0, v23, s[16:17]
	v_cndmask_b32_e64 v38, v39, v38, s[20:21]
	v_fma_f32 v39, v53, v13, v17
	v_mul_f32_e32 v40, s26, v39
	v_cmp_le_f32_e64 s[20:21], 0, v39
	v_cvt_f16_f32_e32 v38, v38
	v_cndmask_b32_e64 v38, 0, v38, s[16:17]
	v_cndmask_b32_e64 v39, v40, v39, s[20:21]
	v_fma_f32 v40, v53, v2, v6
	v_mul_f32_e32 v41, s26, v40
	v_cmp_le_f32_e64 s[20:21], 0, v40
	v_cvt_f16_f32_e32 v39, v39
	v_cndmask_b32_e64 v39, 0, v39, s[16:17]
	v_cndmask_b32_e64 v40, v41, v40, s[20:21]
	v_fma_f32 v41, v53, v3, v7
	v_mul_f32_e32 v42, s26, v41
	v_cmp_le_f32_e64 s[20:21], 0, v41
	v_cvt_f16_f32_e32 v40, v40
	v_pack_b32_f16 v39, v38, v39
	v_cndmask_b32_e64 v41, v42, v41, s[20:21]
	v_fma_f32 v42, v53, v4, v8
	v_mul_f32_e32 v43, s26, v42
	v_cmp_le_f32_e64 s[20:21], 0, v42
	v_cvt_f16_f32_e32 v41, v41
	v_pack_b32_f16 v38, v22, v23
	v_cndmask_b32_e64 v42, v43, v42, s[20:21]
	v_fma_f32 v43, v53, v5, v9
	v_mul_f32_e32 v44, s26, v43
	v_cmp_le_f32_e64 s[20:21], 0, v43
	v_cvt_f16_f32_e32 v42, v42
	v_bitop3_b32 v22, v37, v1, 6 bitop3:0x6c
	v_cndmask_b32_e64 v43, v44, v43, s[20:21]
	v_cvt_f16_f32_e32 v43, v43
	v_cndmask_b32_e64 v40, 0, v40, s[16:17]
	v_cndmask_b32_e64 v44, 0, v41, s[16:17]
	v_cndmask_b32_e64 v41, 0, v42, s[16:17]
	v_cndmask_b32_e64 v42, 0, v43, s[16:17]
	v_lshlrev_b32_e32 v22, 4, v22
	v_pack_b32_f16 v41, v41, v42
	v_pack_b32_f16 v40, v40, v44
	v_lshl_or_b32 v22, v37, 7, v22
	ds_write_b128 v22, v[38:41]
	v_fma_f32 v22, v54, v10, v14
	v_mul_f32_e32 v23, s26, v22
	v_cmp_le_f32_e64 s[16:17], 0, v22
	s_nop 1
	v_cndmask_b32_e64 v22, v23, v22, s[16:17]
	v_fma_f32 v23, v54, v11, v15
	v_mul_f32_e32 v37, s26, v23
	v_cmp_le_f32_e64 s[16:17], 0, v23
	v_cvt_f16_f32_e32 v22, v22
	v_cndmask_b32_e64 v22, v22, 0, s[14:15]
	v_cndmask_b32_e64 v23, v37, v23, s[16:17]
	v_fma_f32 v37, v54, v12, v16
	v_mul_f32_e32 v38, s26, v37
	v_cmp_le_f32_e64 s[16:17], 0, v37
	v_cvt_f16_f32_e32 v23, v23
	v_cndmask_b32_e64 v23, v23, 0, s[14:15]
	v_cndmask_b32_e64 v37, v38, v37, s[16:17]
	v_fma_f32 v38, v54, v13, v17
	v_mul_f32_e32 v39, s26, v38
	v_cmp_le_f32_e64 s[16:17], 0, v38
	v_cvt_f16_f32_e32 v37, v37
	v_cndmask_b32_e64 v37, v37, 0, s[14:15]
	v_cndmask_b32_e64 v38, v39, v38, s[16:17]
	v_fma_f32 v39, v54, v2, v6
	v_mul_f32_e32 v40, s26, v39
	v_cmp_le_f32_e64 s[16:17], 0, v39
	v_cvt_f16_f32_e32 v38, v38
	v_cndmask_b32_e64 v38, v38, 0, s[14:15]
	v_cndmask_b32_e64 v39, v40, v39, s[16:17]
	v_fma_f32 v40, v54, v3, v7
	v_mul_f32_e32 v41, s26, v40
	v_cmp_le_f32_e64 s[16:17], 0, v40
	v_cvt_f16_f32_e32 v39, v39
	v_cndmask_b32_e64 v39, v39, 0, s[14:15]
	v_cndmask_b32_e64 v40, v41, v40, s[16:17]
	v_fma_f32 v41, v54, v4, v8
	v_mul_f32_e32 v42, s26, v41
	v_cmp_le_f32_e64 s[16:17], 0, v41
	v_cvt_f16_f32_e32 v40, v40
	v_cndmask_b32_e64 v40, v40, 0, s[14:15]
	v_cndmask_b32_e64 v41, v42, v41, s[16:17]
	v_fma_f32 v42, v54, v5, v9
	v_mul_f32_e32 v43, s26, v42
	v_cmp_le_f32_e64 s[16:17], 0, v42
	v_cvt_f16_f32_e32 v41, v41
	v_pack_b32_f16 v40, v39, v40
	v_cndmask_b32_e64 v42, v43, v42, s[16:17]
	v_cvt_f16_f32_e32 v42, v42
	v_pack_b32_f16 v39, v37, v38
	v_pack_b32_f16 v38, v22, v23
	v_bitop3_b32 v22, v50, v1, 6 bitop3:0x6c
	v_cndmask_b32_e64 v41, v41, 0, s[14:15]
	v_cndmask_b32_e64 v42, v42, 0, s[14:15]
	v_lshlrev_b32_e32 v22, 4, v22
	v_pack_b32_f16 v41, v41, v42
	v_lshl_or_b32 v22, v50, 7, v22
	ds_write_b128 v22, v[38:41]
	v_fma_f32 v22, v55, v10, v14
	v_mul_f32_e32 v23, s26, v22
	v_cmp_le_f32_e64 s[14:15], 0, v22
	s_nop 1
	v_cndmask_b32_e64 v22, v23, v22, s[14:15]
	v_fma_f32 v23, v55, v11, v15
	v_mul_f32_e32 v37, s26, v23
	v_cmp_le_f32_e64 s[14:15], 0, v23
	v_cvt_f16_f32_e32 v22, v22
	v_cndmask_b32_e64 v22, v22, 0, s[12:13]
	v_cndmask_b32_e64 v23, v37, v23, s[14:15]
	v_fma_f32 v37, v55, v12, v16
	v_mul_f32_e32 v38, s26, v37
	v_cmp_le_f32_e64 s[14:15], 0, v37
	v_cvt_f16_f32_e32 v23, v23
	v_cndmask_b32_e64 v23, v23, 0, s[12:13]
	v_cndmask_b32_e64 v37, v38, v37, s[14:15]
	v_fma_f32 v38, v55, v13, v17
	v_mul_f32_e32 v39, s26, v38
	v_cmp_le_f32_e64 s[14:15], 0, v38
	v_cvt_f16_f32_e32 v37, v37
	v_cndmask_b32_e64 v37, v37, 0, s[12:13]
	v_cndmask_b32_e64 v38, v39, v38, s[14:15]
	v_fma_f32 v39, v55, v2, v6
	v_mul_f32_e32 v40, s26, v39
	v_cmp_le_f32_e64 s[14:15], 0, v39
	v_cvt_f16_f32_e32 v38, v38
	v_cndmask_b32_e64 v38, v38, 0, s[12:13]
	v_cndmask_b32_e64 v39, v40, v39, s[14:15]
	v_fma_f32 v40, v55, v3, v7
	v_mul_f32_e32 v41, s26, v40
	v_cmp_le_f32_e64 s[14:15], 0, v40
	v_cvt_f16_f32_e32 v39, v39
	v_cndmask_b32_e64 v39, v39, 0, s[12:13]
	v_cndmask_b32_e64 v40, v41, v40, s[14:15]
	v_fma_f32 v41, v55, v4, v8
	v_mul_f32_e32 v42, s26, v41
	v_cmp_le_f32_e64 s[14:15], 0, v41
	v_cvt_f16_f32_e32 v40, v40
	v_cndmask_b32_e64 v40, v40, 0, s[12:13]
	v_cndmask_b32_e64 v41, v42, v41, s[14:15]
	v_fma_f32 v42, v55, v5, v9
	v_mul_f32_e32 v43, s26, v42
	v_cmp_le_f32_e64 s[14:15], 0, v42
	v_cvt_f16_f32_e32 v41, v41
	v_pack_b32_f16 v40, v39, v40
	v_cndmask_b32_e64 v42, v43, v42, s[14:15]
	v_cvt_f16_f32_e32 v42, v42
	v_pack_b32_f16 v39, v37, v38
	v_pack_b32_f16 v38, v22, v23
	v_bitop3_b32 v22, v51, v1, 6 bitop3:0x6c
	v_cndmask_b32_e64 v41, v41, 0, s[12:13]
	v_cndmask_b32_e64 v42, v42, 0, s[12:13]
	v_lshlrev_b32_e32 v22, 4, v22
	v_pack_b32_f16 v41, v41, v42
	v_lshl_or_b32 v22, v51, 7, v22
	ds_write_b128 v22, v[38:41]
	v_fma_f32 v22, v56, v10, v14
	v_mul_f32_e32 v23, s26, v22
	v_cmp_le_f32_e64 s[12:13], 0, v22
	s_nop 1
	v_cndmask_b32_e64 v22, v23, v22, s[12:13]
	v_fma_f32 v23, v56, v11, v15
	v_mul_f32_e32 v37, s26, v23
	v_cmp_le_f32_e64 s[12:13], 0, v23
	v_cvt_f16_f32_e32 v22, v22
	v_cndmask_b32_e64 v22, v22, 0, s[10:11]
	v_cndmask_b32_e64 v23, v37, v23, s[12:13]
	v_fma_f32 v37, v56, v12, v16
	v_mul_f32_e32 v38, s26, v37
	v_cmp_le_f32_e64 s[12:13], 0, v37
	v_cvt_f16_f32_e32 v23, v23
	v_cndmask_b32_e64 v23, v23, 0, s[10:11]
	v_cndmask_b32_e64 v37, v38, v37, s[12:13]
	v_fma_f32 v38, v56, v13, v17
	v_mul_f32_e32 v39, s26, v38
	v_cmp_le_f32_e64 s[12:13], 0, v38
	v_cvt_f16_f32_e32 v37, v37
	v_cndmask_b32_e64 v37, v37, 0, s[10:11]
	v_cndmask_b32_e64 v38, v39, v38, s[12:13]
	v_fma_f32 v39, v56, v2, v6
	v_mul_f32_e32 v40, s26, v39
	v_cmp_le_f32_e64 s[12:13], 0, v39
	v_cvt_f16_f32_e32 v38, v38
	v_cndmask_b32_e64 v38, v38, 0, s[10:11]
	v_cndmask_b32_e64 v39, v40, v39, s[12:13]
	v_fma_f32 v40, v56, v3, v7
	v_mul_f32_e32 v41, s26, v40
	v_cmp_le_f32_e64 s[12:13], 0, v40
	v_cvt_f16_f32_e32 v39, v39
	v_cndmask_b32_e64 v39, v39, 0, s[10:11]
	v_cndmask_b32_e64 v40, v41, v40, s[12:13]
	v_fma_f32 v41, v56, v4, v8
	v_mul_f32_e32 v42, s26, v41
	v_cmp_le_f32_e64 s[12:13], 0, v41
	v_cvt_f16_f32_e32 v40, v40
	v_cndmask_b32_e64 v40, v40, 0, s[10:11]
	v_cndmask_b32_e64 v41, v42, v41, s[12:13]
	v_fma_f32 v42, v56, v5, v9
	v_mul_f32_e32 v43, s26, v42
	v_cmp_le_f32_e64 s[12:13], 0, v42
	v_cvt_f16_f32_e32 v41, v41
	v_pack_b32_f16 v40, v39, v40
	v_cndmask_b32_e64 v42, v43, v42, s[12:13]
	v_cvt_f16_f32_e32 v42, v42
	v_pack_b32_f16 v39, v37, v38
	v_pack_b32_f16 v38, v22, v23
	v_bitop3_b32 v22, v52, v1, 6 bitop3:0x6c
	v_cndmask_b32_e64 v41, v41, 0, s[10:11]
	v_cndmask_b32_e64 v42, v42, 0, s[10:11]
	v_lshlrev_b32_e32 v22, 4, v22
	v_pack_b32_f16 v41, v41, v42
	v_lshl_or_b32 v22, v52, 7, v22
	ds_write_b128 v22, v[38:41]
	v_fma_f32 v22, v57, v10, v14
	v_mul_f32_e32 v23, s26, v22
	v_cmp_le_f32_e64 s[10:11], 0, v22
	s_nop 1
	v_cndmask_b32_e64 v22, v23, v22, s[10:11]
	v_fma_f32 v23, v57, v11, v15
	v_mul_f32_e32 v37, s26, v23
	v_cmp_le_f32_e64 s[10:11], 0, v23
	v_cvt_f16_f32_e32 v22, v22
	v_cndmask_b32_e64 v22, v22, 0, s[8:9]
	v_cndmask_b32_e64 v23, v37, v23, s[10:11]
	v_fma_f32 v37, v57, v12, v16
	v_mul_f32_e32 v38, s26, v37
	v_cmp_le_f32_e64 s[10:11], 0, v37
	v_cvt_f16_f32_e32 v23, v23
	v_cndmask_b32_e64 v23, v23, 0, s[8:9]
	v_cndmask_b32_e64 v37, v38, v37, s[10:11]
	v_fma_f32 v38, v57, v13, v17
	v_mul_f32_e32 v39, s26, v38
	v_cmp_le_f32_e64 s[10:11], 0, v38
	v_cvt_f16_f32_e32 v37, v37
	v_cndmask_b32_e64 v37, v37, 0, s[8:9]
	v_cndmask_b32_e64 v38, v39, v38, s[10:11]
	v_fma_f32 v39, v57, v2, v6
	v_mul_f32_e32 v40, s26, v39
	v_cmp_le_f32_e64 s[10:11], 0, v39
	v_cvt_f16_f32_e32 v38, v38
	v_cndmask_b32_e64 v38, v38, 0, s[8:9]
	v_cndmask_b32_e64 v39, v40, v39, s[10:11]
	v_fma_f32 v40, v57, v3, v7
	v_mul_f32_e32 v41, s26, v40
	v_cmp_le_f32_e64 s[10:11], 0, v40
	v_cvt_f16_f32_e32 v39, v39
	v_cndmask_b32_e64 v39, v39, 0, s[8:9]
	v_cndmask_b32_e64 v40, v41, v40, s[10:11]
	v_fma_f32 v41, v57, v4, v8
	v_mul_f32_e32 v42, s26, v41
	v_cmp_le_f32_e64 s[10:11], 0, v41
	v_cvt_f16_f32_e32 v40, v40
	v_cndmask_b32_e64 v40, v40, 0, s[8:9]
	v_cndmask_b32_e64 v41, v42, v41, s[10:11]
	v_fma_f32 v42, v57, v5, v9
	v_mul_f32_e32 v43, s26, v42
	v_cmp_le_f32_e64 s[10:11], 0, v42
	v_cvt_f16_f32_e32 v41, v41
	v_pack_b32_f16 v40, v39, v40
	v_cndmask_b32_e64 v42, v43, v42, s[10:11]
	v_cvt_f16_f32_e32 v42, v42
	v_pack_b32_f16 v39, v37, v38
	v_pack_b32_f16 v38, v22, v23
	v_bitop3_b32 v22, v35, v1, 6 bitop3:0x6c
	v_cndmask_b32_e64 v41, v41, 0, s[8:9]
	v_cndmask_b32_e64 v42, v42, 0, s[8:9]
	v_lshlrev_b32_e32 v22, 4, v22
	v_pack_b32_f16 v41, v41, v42
	v_lshl_or_b32 v22, v35, 7, v22
	ds_write_b128 v22, v[38:41]
	v_fma_f32 v22, v36, v10, v14
	v_mul_f32_e32 v23, s26, v22
	v_cmp_le_f32_e64 s[8:9], 0, v22
	s_nop 1
	v_cndmask_b32_e64 v22, v23, v22, s[8:9]
	v_fma_f32 v23, v36, v11, v15
	v_mul_f32_e32 v35, s26, v23
	v_cmp_le_f32_e64 s[8:9], 0, v23
	v_cvt_f16_f32_e32 v22, v22
	v_cndmask_b32_e64 v22, v22, 0, s[6:7]
	v_cndmask_b32_e64 v23, v35, v23, s[8:9]
	v_fma_f32 v35, v36, v12, v16
	v_mul_f32_e32 v37, s26, v35
	v_cmp_le_f32_e64 s[8:9], 0, v35
	v_cvt_f16_f32_e32 v23, v23
	v_cndmask_b32_e64 v23, v23, 0, s[6:7]
	v_cndmask_b32_e64 v35, v37, v35, s[8:9]
	v_fma_f32 v37, v36, v13, v17
	v_mul_f32_e32 v38, s26, v37
	v_cmp_le_f32_e64 s[8:9], 0, v37
	v_cvt_f16_f32_e32 v35, v35
	v_cndmask_b32_e64 v35, v35, 0, s[6:7]
	v_cndmask_b32_e64 v37, v38, v37, s[8:9]
	v_fma_f32 v38, v36, v2, v6
	v_mul_f32_e32 v39, s26, v38
	v_cmp_le_f32_e64 s[8:9], 0, v38
	v_cvt_f16_f32_e32 v37, v37
	v_cndmask_b32_e64 v37, v37, 0, s[6:7]
	v_cndmask_b32_e64 v38, v39, v38, s[8:9]
	v_fma_f32 v39, v36, v3, v7
	v_mul_f32_e32 v40, s26, v39
	v_cmp_le_f32_e64 s[8:9], 0, v39
	v_cvt_f16_f32_e32 v38, v38
	v_pack_b32_f16 v37, v35, v37
	v_cndmask_b32_e64 v39, v40, v39, s[8:9]
	v_fma_f32 v40, v36, v4, v8
	v_mul_f32_e32 v41, s26, v40
	v_cmp_le_f32_e64 s[8:9], 0, v40
	v_fma_f32 v36, v36, v5, v9
	v_cvt_f16_f32_e32 v39, v39
	v_cndmask_b32_e64 v40, v41, v40, s[8:9]
	v_mul_f32_e32 v41, s26, v36
	v_cmp_le_f32_e64 s[8:9], 0, v36
	v_cvt_f16_f32_e32 v40, v40
	v_cndmask_b32_e64 v38, v38, 0, s[6:7]
	v_cndmask_b32_e64 v36, v41, v36, s[8:9]
	v_cvt_f16_f32_e32 v36, v36
	v_cndmask_b32_e64 v41, v39, 0, s[6:7]
	v_cndmask_b32_e64 v39, v40, 0, s[6:7]
	v_pack_b32_f16 v38, v38, v41
	v_cndmask_b32_e64 v36, v36, 0, s[6:7]
	v_pack_b32_f16 v39, v39, v36
	v_pack_b32_f16 v36, v22, v23
	v_bitop3_b32 v22, v33, v1, 6 bitop3:0x6c
	v_lshlrev_b32_e32 v22, 4, v22
	v_fma_f32 v23, v34, v10, v14
	v_lshl_or_b32 v22, v33, 7, v22
	v_mul_f32_e32 v33, s26, v23
	v_cmp_le_f32_e64 s[6:7], 0, v23
	ds_write_b128 v22, v[36:39]
	v_bitop3_b32 v22, v32, 64, v30 bitop3:0xc8
	v_cndmask_b32_e64 v23, v33, v23, s[6:7]
	v_fma_f32 v33, v34, v11, v15
	v_mul_f32_e32 v35, s26, v33
	v_cmp_le_f32_e64 s[6:7], 0, v33
	v_cvt_f16_f32_e32 v23, v23
	s_nop 0
	v_cndmask_b32_e64 v33, v35, v33, s[6:7]
	v_fma_f32 v35, v34, v12, v16
	v_mul_f32_e32 v36, s26, v35
	v_cmp_le_f32_e64 s[6:7], 0, v35
	v_cvt_f16_f32_e32 v33, v33
	s_nop 0
	v_cndmask_b32_e64 v35, v36, v35, s[6:7]
	v_fma_f32 v36, v34, v13, v17
	v_mul_f32_e32 v37, s26, v36
	v_cmp_le_f32_e64 s[6:7], 0, v36
	v_cvt_f16_f32_e32 v35, v35
	s_nop 0
	v_cndmask_b32_e64 v36, v37, v36, s[6:7]
	v_cvt_f16_f32_e32 v36, v36
	v_cmp_eq_u32_e64 s[6:7], 0, v22
	s_nop 1
	v_cndmask_b32_e64 v22, v23, 0, s[6:7]
	v_cndmask_b32_e64 v23, v33, 0, s[6:7]
	v_cndmask_b32_e64 v33, v35, 0, s[6:7]
	v_cndmask_b32_e64 v35, v36, 0, s[6:7]
	v_fma_f32 v36, v34, v2, v6
	v_mul_f32_e32 v37, s26, v36
	v_cmp_le_f32_e64 s[8:9], 0, v36
	v_pack_b32_f16 v35, v33, v35
	s_nop 0
	v_cndmask_b32_e64 v36, v37, v36, s[8:9]
	v_fma_f32 v37, v34, v3, v7
	v_mul_f32_e32 v38, s26, v37
	v_cmp_le_f32_e64 s[8:9], 0, v37
	v_cvt_f16_f32_e32 v36, v36
	v_cndmask_b32_e64 v36, v36, 0, s[6:7]
	v_cndmask_b32_e64 v37, v38, v37, s[8:9]
	v_fma_f32 v38, v34, v4, v8
	v_mul_f32_e32 v39, s26, v38
	v_cmp_le_f32_e64 s[8:9], 0, v38
	v_fma_f32 v34, v34, v5, v9
	v_cvt_f16_f32_e32 v37, v37
	v_cndmask_b32_e64 v38, v39, v38, s[8:9]
	v_mul_f32_e32 v39, s26, v34
	v_cmp_le_f32_e64 s[8:9], 0, v34
	v_cvt_f16_f32_e32 v38, v38
	s_nop 0
	v_cndmask_b32_e64 v34, v39, v34, s[8:9]
	v_cvt_f16_f32_e32 v34, v34
	v_cndmask_b32_e64 v39, v37, 0, s[6:7]
	v_cndmask_b32_e64 v37, v38, 0, s[6:7]
	v_pack_b32_f16 v36, v36, v39
	v_cndmask_b32_e64 v34, v34, 0, s[6:7]
	v_pack_b32_f16 v37, v37, v34
	v_pack_b32_f16 v34, v22, v23
	v_bitop3_b32 v22, v31, v1, 6 bitop3:0x6c
	v_lshlrev_b32_e32 v22, 4, v22
	v_lshl_or_b32 v22, v31, 7, v22
	v_fma_f32 v23, v29, v10, v14
	ds_write_b128 v22, v[34:37]
	v_bitop3_b32 v22, v32, s29, v30 bitop3:0xc8
	v_mul_f32_e32 v30, s26, v23
	v_cmp_le_f32_e64 s[6:7], 0, v23
	s_nop 1
	v_cndmask_b32_e64 v23, v30, v23, s[6:7]
	v_fma_f32 v30, v29, v11, v15
	v_mul_f32_e32 v31, s26, v30
	v_cmp_le_f32_e64 s[6:7], 0, v30
	v_cvt_f16_f32_e32 v23, v23
	s_nop 0
	v_cndmask_b32_e64 v30, v31, v30, s[6:7]
	v_fma_f32 v31, v29, v12, v16
	v_mul_f32_e32 v32, s26, v31
	v_cmp_le_f32_e64 s[6:7], 0, v31
	v_cvt_f16_f32_e32 v30, v30
	s_nop 0
	v_cndmask_b32_e64 v31, v32, v31, s[6:7]
	v_fma_f32 v32, v29, v13, v17
	v_mul_f32_e32 v33, s26, v32
	v_cmp_le_f32_e64 s[6:7], 0, v32
	v_cvt_f16_f32_e32 v31, v31
	s_nop 0
	v_cndmask_b32_e64 v32, v33, v32, s[6:7]
	v_cvt_f16_f32_e32 v32, v32
	v_cmp_eq_u32_e64 s[6:7], 0, v22
	s_nop 1
	v_cndmask_b32_e64 v22, v23, 0, s[6:7]
	v_cndmask_b32_e64 v23, v30, 0, s[6:7]
	v_cndmask_b32_e64 v30, v31, 0, s[6:7]
	v_cndmask_b32_e64 v31, v32, 0, s[6:7]
	v_fma_f32 v32, v29, v2, v6
	v_mul_f32_e32 v33, s26, v32
	v_cmp_le_f32_e64 s[8:9], 0, v32
	v_pack_b32_f16 v31, v30, v31
	v_pack_b32_f16 v30, v22, v23
	v_cndmask_b32_e64 v32, v33, v32, s[8:9]
	v_fma_f32 v33, v29, v3, v7
	v_mul_f32_e32 v34, s26, v33
	v_cmp_le_f32_e64 s[8:9], 0, v33
	v_cvt_f16_f32_e32 v32, v32
	v_bitop3_b32 v22, v26, v1, 6 bitop3:0x6c
	v_cndmask_b32_e64 v33, v34, v33, s[8:9]
	v_fma_f32 v34, v29, v4, v8
	v_mul_f32_e32 v35, s26, v34
	v_cmp_le_f32_e64 s[8:9], 0, v34
	v_fma_f32 v29, v29, v5, v9
	v_cvt_f16_f32_e32 v33, v33
	v_cndmask_b32_e64 v34, v35, v34, s[8:9]
	v_mul_f32_e32 v35, s26, v29
	v_cmp_le_f32_e64 s[8:9], 0, v29
	v_cvt_f16_f32_e32 v34, v34
	v_cndmask_b32_e64 v32, v32, 0, s[6:7]
	v_cndmask_b32_e64 v29, v35, v29, s[8:9]
	v_cvt_f16_f32_e32 v29, v29
	v_cndmask_b32_e64 v35, v33, 0, s[6:7]
	v_cndmask_b32_e64 v33, v34, 0, s[6:7]
	v_lshlrev_b32_e32 v22, 4, v22
	v_cndmask_b32_e64 v29, v29, 0, s[6:7]
	v_pack_b32_f16 v33, v33, v29
	v_pack_b32_f16 v32, v32, v35
	v_lshl_or_b32 v22, v26, 7, v22
	ds_write_b128 v22, v[30:33]
	s_and_saveexec_b64 s[6:7], s[4:5]
	s_cbranch_execz .LBB3_2
	v_cndmask_b32_e64 v22, 0, v28, s[18:19]
	v_or_b32_e32 v22, s28, v22
	v_cndmask_b32_e64 v23, 0, v27, s[18:19]
	v_lshl_add_u32 v22, v22, 6, v23
	v_ashrrev_i32_e32 v23, 31, v22
	v_lshl_add_u64 v[22:23], v[22:23], 2, s[24:25]
	global_load_dword v22, v[22:23], off
	v_bitop3_b32 v26, v24, v1, 6 bitop3:0x6c
	v_lshlrev_b32_e32 v30, 4, v26
	v_and_b32_e32 v23, 0x100, v25
	s_waitcnt vmcnt(0)
	v_fma_f32 v26, v22, v10, v14
	v_fma_f32 v27, v22, v11, v15
	v_mul_f32_e32 v34, s26, v26
	v_cmp_le_f32_e64 s[4:5], 0, v26
	v_fma_f32 v28, v22, v12, v16
	v_mul_f32_e32 v35, s26, v27
	v_cndmask_b32_e64 v26, v34, v26, s[4:5]
	v_cmp_le_f32_e64 s[4:5], 0, v27
	v_fma_f32 v29, v22, v13, v17
	v_mul_f32_e32 v36, s26, v28
	v_cndmask_b32_e64 v27, v35, v27, s[4:5]
	v_cmp_le_f32_e64 s[4:5], 0, v28
	v_fma_f32 v31, v22, v2, v6
	v_mul_f32_e32 v37, s26, v29
	v_cndmask_b32_e64 v28, v36, v28, s[4:5]
	v_cmp_le_f32_e64 s[4:5], 0, v29
	v_fma_f32 v32, v22, v3, v7
	v_mul_f32_e32 v38, s26, v31
	v_cndmask_b32_e64 v29, v37, v29, s[4:5]
	v_cmp_le_f32_e64 s[4:5], 0, v31
	v_fma_f32 v33, v22, v4, v8
	v_mul_f32_e32 v39, s26, v32
	v_cndmask_b32_e64 v31, v38, v31, s[4:5]
	v_cmp_le_f32_e64 s[4:5], 0, v32
	v_fma_f32 v22, v22, v5, v9
	v_mul_f32_e32 v40, s26, v33
	v_cndmask_b32_e64 v32, v39, v32, s[4:5]
	v_cmp_le_f32_e64 s[4:5], 0, v33
	v_mul_f32_e32 v41, s26, v22
	v_cvt_f16_f32_e32 v26, v26
	v_cndmask_b32_e64 v33, v40, v33, s[4:5]
	v_cmp_le_f32_e64 s[4:5], 0, v22
	v_cvt_f16_f32_e32 v27, v27
	v_cvt_f16_f32_e32 v28, v28
	v_cndmask_b32_e64 v22, v41, v22, s[4:5]
	v_cvt_f16_f32_e32 v29, v29
	v_cvt_f16_f32_e32 v31, v31
	v_cvt_f16_f32_e32 v32, v32
	v_cvt_f16_f32_e32 v33, v33
	v_cvt_f16_f32_e32 v22, v22
	v_cmp_eq_u32_e64 s[4:5], 0, v23
	s_nop 1
	v_cndmask_b32_e64 v23, v26, 0, s[4:5]
	v_cndmask_b32_e64 v26, v27, 0, s[4:5]
	v_cndmask_b32_e64 v27, v28, 0, s[4:5]
	v_cndmask_b32_e64 v34, v29, 0, s[4:5]
	v_cndmask_b32_e64 v28, v31, 0, s[4:5]
	v_cndmask_b32_e64 v31, v32, 0, s[4:5]
	v_cndmask_b32_e64 v29, v33, 0, s[4:5]
	v_cndmask_b32_e64 v22, v22, 0, s[4:5]
	v_pack_b32_f16 v29, v29, v22
	v_pack_b32_f16 v28, v28, v31
	v_pack_b32_f16 v27, v27, v34
	v_pack_b32_f16 v26, v23, v26
	v_lshl_or_b32 v22, v24, 7, v30
	ds_write_b128 v22, v[26:29]
